# F1 + up-proj epilogue part 1: cross-lane sums via v_permlane16_swap/v_permlane32_swap (VALU) instead of ds_bpermute_b32 LDS round trips (32 sites); key-loop 64-byte phase unchanged
# speedup vs baseline: 1.0089x; 1.0089x over previous
.LBB0_408:
	v_and_b32_e32 v115, 64, v221
	v_xor_b32_e32 v114, 16, v221
	v_add_u32_e32 v115, 64, v115
	v_cmp_lt_i32_e32 vcc, v114, v115
	v_xor_b32_e32 v117, 32, v221
	v_cmp_lt_u32_e64 s[10:11], 15, v112
	v_cndmask_b32_e32 v114, v221, v114, vcc
	v_lshlrev_b32_e32 v114, 2, v114
	v_mov_b32_e32 v116, v113
	s_nop 1
	v_permlane16_swap_b32_e32 v116, v113
	v_cmp_lt_i32_e32 vcc, v117, v115
	v_cmp_gt_u32_e64 s[12:13], 16, v112
	s_waitcnt lgkmcnt(0)
	v_add_f32_e32 v113, v113, v116
	v_cndmask_b32_e32 v115, v221, v117, vcc
	v_lshlrev_b32_e32 v115, 2, v115
	v_mov_b32_e32 v117, v113
	s_nop 1
	v_permlane32_swap_b32_e32 v117, v113
	v_lshl_add_u32 v116, v231, 4, s88
	s_and_saveexec_b64 s[8:9], s[12:13]
	s_cbranch_execz .LBB0_410
	s_waitcnt lgkmcnt(0)
	v_add_f32_e32 v112, v113, v117
	ds_write_b32 v116, v112

.LBB0_418:
	v_mov_b32_e32 v112, v117
	s_nop 1
	v_permlane16_swap_b32_e32 v112, v117
	s_waitcnt lgkmcnt(0)
	v_add_f32_e32 v112, v117, v112
	v_mov_b32_e32 v113, v112
	s_nop 1
	v_permlane32_swap_b32_e32 v113, v112
	s_and_saveexec_b64 s[14:15], s[12:13]
	s_cbranch_execz .LBB0_420
	s_waitcnt lgkmcnt(0)
	v_add_f32_e32 v112, v112, v113
	ds_write_b32 v116, v112 offset:256

.LBB0_428:
	v_mov_b32_e32 v112, v117
	s_nop 1
	v_permlane16_swap_b32_e32 v112, v117
	s_waitcnt lgkmcnt(0)
	v_add_f32_e32 v112, v117, v112
	v_mov_b32_e32 v113, v112
	s_nop 1
	v_permlane32_swap_b32_e32 v113, v112
	s_and_saveexec_b64 s[14:15], s[12:13]
	s_cbranch_execz .LBB0_430
	s_waitcnt lgkmcnt(0)
	v_add_f32_e32 v112, v112, v113
	ds_write_b32 v116, v112 offset:512

.LBB0_438:
	v_mov_b32_e32 v112, v117
	s_nop 1
	v_permlane16_swap_b32_e32 v112, v117
	s_waitcnt lgkmcnt(0)
	v_add_f32_e32 v112, v117, v112
	v_mov_b32_e32 v113, v112
	s_nop 1
	v_permlane32_swap_b32_e32 v113, v112
	s_and_saveexec_b64 s[14:15], s[12:13]
	s_cbranch_execz .LBB0_440
	s_waitcnt lgkmcnt(0)
	v_add_f32_e32 v112, v112, v113
	ds_write_b32 v116, v112 offset:768

.LBB0_448:
	v_mov_b32_e32 v112, v118
	s_nop 1
	v_permlane16_swap_b32_e32 v112, v118
	v_add_u32_e32 v227, 0x80, v231
	s_waitcnt lgkmcnt(0)
	v_add_f32_e32 v112, v118, v112
	v_mov_b32_e32 v113, v112
	s_nop 1
	v_permlane32_swap_b32_e32 v113, v112
	s_and_saveexec_b64 s[14:15], s[12:13]
	s_cbranch_execz .LBB0_450
	s_waitcnt lgkmcnt(0)
	v_add_f32_e32 v112, v112, v113
	v_lshl_add_u32 v113, v227, 4, s88
	ds_write_b32 v113, v112

.LBB0_458:
	v_mov_b32_e32 v112, v118
	s_nop 1
	v_permlane16_swap_b32_e32 v112, v118
	s_waitcnt lgkmcnt(0)
	v_add_f32_e32 v112, v118, v112
	v_mov_b32_e32 v113, v112
	s_nop 1
	v_permlane32_swap_b32_e32 v113, v112
	s_and_saveexec_b64 s[14:15], s[12:13]
	s_cbranch_execz .LBB0_460
	s_waitcnt lgkmcnt(0)
	v_add_f32_e32 v112, v112, v113
	ds_write_b32 v116, v112 offset:2304

.LBB0_468:
	v_mov_b32_e32 v112, v118
	s_nop 1
	v_permlane16_swap_b32_e32 v112, v118
	s_waitcnt lgkmcnt(0)
	v_add_f32_e32 v112, v118, v112
	v_mov_b32_e32 v113, v112
	s_nop 1
	v_permlane32_swap_b32_e32 v113, v112
	s_and_saveexec_b64 s[14:15], s[12:13]
	s_cbranch_execz .LBB0_470
	s_waitcnt lgkmcnt(0)
	v_add_f32_e32 v112, v112, v113
	ds_write_b32 v116, v112 offset:2560

.LBB0_478:
	v_mov_b32_e32 v112, v117
	s_nop 1
	v_permlane16_swap_b32_e32 v112, v117
	s_waitcnt lgkmcnt(0)
	v_add_f32_e32 v113, v117, v112
	v_mov_b32_e32 v114, v113
	s_nop 1
	v_permlane32_swap_b32_e32 v114, v113
	v_lshlrev_b32_e32 v112, 4, v231
	s_and_saveexec_b64 s[12:13], s[10:11]
	s_xor_b64 s[10:11], exec, s[12:13]
	v_lshlrev_b32_e32 v112, 4, v231
	s_andn2_saveexec_b64 s[10:11], s[10:11]
	s_cbranch_execz .LBB0_482
	s_waitcnt lgkmcnt(0)
	v_add_f32_e32 v113, v113, v114
	v_add_u32_e32 v114, s88, v112
	ds_write_b32 v114, v113 offset:2816
